# v47 + G5 epilogue rewritten by hand: silu(rs*a)*(rs*b) computed as (a*b)*rcp((1+exp2(a*rs*-log2e))/rs^2) in f32 (39 VALU per 8 outputs instead of ~57), no epilogue vmcnt(0), software-pipelined bpermut
# speedup vs baseline: 1.0135x; 1.0069x over previous
; __device__ __forceinline__ unsigned cvt_pk_bf16(float lo, float hi) { const f32x2c_t v = {lo, hi}; return __builtin_bit_cast(unsigned, __builtin_convertvector(v, bf16x2c_t)); }
; __device__ __forceinline__ float silu_f(float a) { return a * __builtin_amdgcn_rcpf(1.0f + __builtin_amdgcn_exp2f(a * -1.4426950408889634f)); }
;     __device__ __forceinline__ void operator()(const f32x4 (&acc)[2][2][4][2], const Unit& u, int wr, int wc, int fr, int fq) const {
;     ...
;         for (int ai = 0; ai < 2; ++ai) {
; #pragma unroll
;             for (int m = 0; m < 4; ++m) { const int row = row0 + ai * HALF + m * 16; const float rs = rs8[ai][m];
;                 const f32x4 a0 = acc[ai][0][m][0] * rs, a1 = acc[ai][0][m][1] * rs, b0 = acc[ai][1][m][0] * rs, b1 = acc[ai][1][m][1] * rs;
;                 f32x4 g0, g1;
; #pragma unroll
;                 for (int j = 0; j < 4; ++j) { g0[j] = silu_f(a0[j]) * b0[j]; g1[j] = silu_f(a1[j]) * b1[j]; }
;                 u32x4 w; w.x = cvt_pk_bf16(g0[0], g0[1]); w.y = cvt_pk_bf16(g0[2], g0[3]); w.z = cvt_pk_bf16(g1[0], g1[1]); w.w = cvt_pk_bf16(g1[2], g1[3]);
;                 w = lane_perm(w, qs4); u32x4* dst = (u32x4*)(O + (size_t)(rowS + ai * HALF + m * 16) * ldo + colS); (void)row;
;                 if constexpr (MOE) __builtin_nontemporal_store(w, dst); else *dst = w; } }
.LBB0_1731:
	s_lshl_b32 s6, s38, 8
	s_add_i32 s6, s6, s54
	s_mul_hi_i32 s7, s36, 0x92492493
	v_readlane_b32 s40, v254, 36
	s_add_i32 s7, s7, s36
	v_readlane_b32 s41, v254, 37
	v_or_b32_e32 v147, s6, v155
	s_lshr_b32 s6, s7, 31
	s_lshr_b32 s7, s7, 4
	v_mov_b64_e32 v[140:141], s[40:41]
	s_add_i32 s29, s7, s6
	v_mad_i64_i32 v[170:171], s[6:7], v147, s60, v[140:141]
	s_mul_i32 s29, s29, 28
	s_sub_i32 s6, s36, s29
	v_lshl_or_b32 v142, s6, 7, v157
	v_ashrrev_i32_e32 v143, 31, v142
	v_lshlrev_b64 v[142:143], 1, v[142:143]
	v_lshl_add_u64 v[170:171], v[170:171], 0, v[142:143]
	v_mul_f32_e32 v248, 0xbfb8aa3b, v247
	v_mul_f32_e32 v250, v247, v247
	v_rcp_f32_e32 v250, v250
	v_pk_mul_f32 v[118:119], v[118:119], v[126:127]
	v_pk_mul_f32 v[120:121], v[120:121], v[128:129]
	v_pk_mul_f32 v[114:115], v[114:115], v[122:123]
	v_pk_mul_f32 v[116:117], v[116:117], v[124:125]
	v_pk_mul_f32 v[126:127], v[126:127], v[248:249] op_sel_hi:[1,0]
	v_pk_mul_f32 v[128:129], v[128:129], v[248:249] op_sel_hi:[1,0]
	v_pk_mul_f32 v[122:123], v[122:123], v[248:249] op_sel_hi:[1,0]
	v_pk_mul_f32 v[124:125], v[124:125], v[248:249] op_sel_hi:[1,0]
	v_exp_f32_e32 v126, v126
	v_exp_f32_e32 v127, v127
	v_exp_f32_e32 v128, v128
	v_exp_f32_e32 v129, v129
	v_exp_f32_e32 v122, v122
	v_exp_f32_e32 v123, v123
	v_exp_f32_e32 v124, v124
	v_exp_f32_e32 v125, v125
	v_pk_fma_f32 v[126:127], v[126:127], v[250:251], v[250:251] op_sel_hi:[1,0,0]
	v_pk_fma_f32 v[128:129], v[128:129], v[250:251], v[250:251] op_sel_hi:[1,0,0]
	v_pk_fma_f32 v[122:123], v[122:123], v[250:251], v[250:251] op_sel_hi:[1,0,0]
	v_pk_fma_f32 v[124:125], v[124:125], v[250:251], v[250:251] op_sel_hi:[1,0,0]
	v_rcp_f32_e32 v126, v126
	v_rcp_f32_e32 v127, v127
	v_rcp_f32_e32 v128, v128
	v_rcp_f32_e32 v129, v129
	v_rcp_f32_e32 v122, v122
	v_rcp_f32_e32 v123, v123
	v_rcp_f32_e32 v124, v124
	v_rcp_f32_e32 v125, v125
	v_pk_mul_f32 v[118:119], v[118:119], v[126:127]
	v_pk_mul_f32 v[120:121], v[120:121], v[128:129]
	v_pk_mul_f32 v[114:115], v[114:115], v[122:123]
	v_pk_mul_f32 v[116:117], v[116:117], v[124:125]
	v_cvt_pk_bf16_f32 v126, v118, v119
	v_cvt_pk_bf16_f32 v127, v120, v121
	v_cvt_pk_bf16_f32 v128, v114, v115
	v_cvt_pk_bf16_f32 v129, v116, v117
	ds_bpermute_b32 v122, v156, v126
	ds_bpermute_b32 v123, v156, v127
	ds_bpermute_b32 v124, v156, v128
	ds_bpermute_b32 v125, v156, v129
	v_mov_b32_e32 v140, v170
	v_mov_b32_e32 v141, v171
	v_mul_f32_e32 v248, 0xbfb8aa3b, v246
	v_mul_f32_e32 v250, v246, v246
	v_rcp_f32_e32 v250, v250
	v_pk_mul_f32 v[102:103], v[102:103], v[110:111]
	v_pk_mul_f32 v[104:105], v[104:105], v[112:113]
	v_pk_mul_f32 v[98:99], v[98:99], v[106:107]
	v_pk_mul_f32 v[100:101], v[100:101], v[108:109]
	v_pk_mul_f32 v[110:111], v[110:111], v[248:249] op_sel_hi:[1,0]
	v_pk_mul_f32 v[112:113], v[112:113], v[248:249] op_sel_hi:[1,0]
	v_pk_mul_f32 v[106:107], v[106:107], v[248:249] op_sel_hi:[1,0]
	v_pk_mul_f32 v[108:109], v[108:109], v[248:249] op_sel_hi:[1,0]
	v_exp_f32_e32 v110, v110
	v_exp_f32_e32 v111, v111
	v_exp_f32_e32 v112, v112
	v_exp_f32_e32 v113, v113
	v_exp_f32_e32 v106, v106
	v_exp_f32_e32 v107, v107
	v_exp_f32_e32 v108, v108
	v_exp_f32_e32 v109, v109
	v_pk_fma_f32 v[110:111], v[110:111], v[250:251], v[250:251] op_sel_hi:[1,0,0]
	v_pk_fma_f32 v[112:113], v[112:113], v[250:251], v[250:251] op_sel_hi:[1,0,0]
	v_pk_fma_f32 v[106:107], v[106:107], v[250:251], v[250:251] op_sel_hi:[1,0,0]
	v_pk_fma_f32 v[108:109], v[108:109], v[250:251], v[250:251] op_sel_hi:[1,0,0]
	v_rcp_f32_e32 v110, v110
	v_rcp_f32_e32 v111, v111
	v_rcp_f32_e32 v112, v112
	v_rcp_f32_e32 v113, v113
	v_rcp_f32_e32 v106, v106
	v_rcp_f32_e32 v107, v107
	v_rcp_f32_e32 v108, v108
	v_rcp_f32_e32 v109, v109
	v_pk_mul_f32 v[102:103], v[102:103], v[110:111]
	v_pk_mul_f32 v[104:105], v[104:105], v[112:113]
	v_pk_mul_f32 v[98:99], v[98:99], v[106:107]
	v_pk_mul_f32 v[100:101], v[100:101], v[108:109]
	s_waitcnt lgkmcnt(0)
	global_store_dwordx4 v[140:141], v[122:125], off nt
	v_cvt_pk_bf16_f32 v110, v102, v103
	v_cvt_pk_bf16_f32 v111, v104, v105
	v_cvt_pk_bf16_f32 v112, v98, v99
	v_cvt_pk_bf16_f32 v113, v100, v101
	ds_bpermute_b32 v106, v156, v110
	ds_bpermute_b32 v107, v156, v111
	ds_bpermute_b32 v108, v156, v112
	ds_bpermute_b32 v109, v156, v113
	v_add_co_u32_e32 v142, vcc, 0x1c000, v170
	v_addc_co_u32_e32 v143, vcc, 0, v171, vcc
	v_mul_f32_e32 v248, 0xbfb8aa3b, v245
	v_mul_f32_e32 v250, v245, v245
	v_rcp_f32_e32 v250, v250
	v_pk_mul_f32 v[86:87], v[86:87], v[94:95]
	v_pk_mul_f32 v[88:89], v[88:89], v[96:97]
	v_pk_mul_f32 v[82:83], v[82:83], v[90:91]
	v_pk_mul_f32 v[84:85], v[84:85], v[92:93]
	v_pk_mul_f32 v[94:95], v[94:95], v[248:249] op_sel_hi:[1,0]
	v_pk_mul_f32 v[96:97], v[96:97], v[248:249] op_sel_hi:[1,0]
	v_pk_mul_f32 v[90:91], v[90:91], v[248:249] op_sel_hi:[1,0]
	v_pk_mul_f32 v[92:93], v[92:93], v[248:249] op_sel_hi:[1,0]
	v_exp_f32_e32 v94, v94
	v_exp_f32_e32 v95, v95
	v_exp_f32_e32 v96, v96
	v_exp_f32_e32 v97, v97
	v_exp_f32_e32 v90, v90
	v_exp_f32_e32 v91, v91
	v_exp_f32_e32 v92, v92
	v_exp_f32_e32 v93, v93
	v_pk_fma_f32 v[94:95], v[94:95], v[250:251], v[250:251] op_sel_hi:[1,0,0]
	v_pk_fma_f32 v[96:97], v[96:97], v[250:251], v[250:251] op_sel_hi:[1,0,0]
	v_pk_fma_f32 v[90:91], v[90:91], v[250:251], v[250:251] op_sel_hi:[1,0,0]
	v_pk_fma_f32 v[92:93], v[92:93], v[250:251], v[250:251] op_sel_hi:[1,0,0]
	v_rcp_f32_e32 v94, v94
	v_rcp_f32_e32 v95, v95
	v_rcp_f32_e32 v96, v96
	v_rcp_f32_e32 v97, v97
	v_rcp_f32_e32 v90, v90
	v_rcp_f32_e32 v91, v91
	v_rcp_f32_e32 v92, v92
	v_rcp_f32_e32 v93, v93
	v_pk_mul_f32 v[86:87], v[86:87], v[94:95]
	v_pk_mul_f32 v[88:89], v[88:89], v[96:97]
	v_pk_mul_f32 v[82:83], v[82:83], v[90:91]
	v_pk_mul_f32 v[84:85], v[84:85], v[92:93]
	s_waitcnt lgkmcnt(0)
; __device__ __forceinline__ unsigned cvt_pk_bf16(float lo, float hi) { const f32x2c_t v = {lo, hi}; return __builtin_bit_cast(unsigned, __builtin_convertvector(v, bf16x2c_t)); }
; __device__ __forceinline__ float silu_f(float a) { return a * __builtin_amdgcn_rcpf(1.0f + __builtin_amdgcn_exp2f(a * -1.4426950408889634f)); }
;     __device__ __forceinline__ void operator()(const f32x4 (&acc)[2][2][4][2], const Unit& u, int wr, int wc, int fr, int fq) const {
;     ...
;         for (int ai = 0; ai < 2; ++ai) {
; #pragma unroll
;             for (int m = 0; m < 4; ++m) { const int row = row0 + ai * HALF + m * 16; const float rs = rs8[ai][m];
;                 const f32x4 a0 = acc[ai][0][m][0] * rs, a1 = acc[ai][0][m][1] * rs, b0 = acc[ai][1][m][0] * rs, b1 = acc[ai][1][m][1] * rs;
;                 f32x4 g0, g1;
; #pragma unroll
;                 for (int j = 0; j < 4; ++j) { g0[j] = silu_f(a0[j]) * b0[j]; g1[j] = silu_f(a1[j]) * b1[j]; }
;                 u32x4 w; w.x = cvt_pk_bf16(g0[0], g0[1]); w.y = cvt_pk_bf16(g0[2], g0[3]); w.z = cvt_pk_bf16(g1[0], g1[1]); w.w = cvt_pk_bf16(g1[2], g1[3]);
;                 w = lane_perm(w, qs4); u32x4* dst = (u32x4*)(O + (size_t)(rowS + ai * HALF + m * 16) * ldo + colS); (void)row;
;                 if constexpr (MOE) __builtin_nontemporal_store(w, dst); else *dst = w; } }
	global_store_dwordx4 v[142:143], v[106:109], off nt
	v_cvt_pk_bf16_f32 v94, v86, v87
	v_cvt_pk_bf16_f32 v95, v88, v89
	v_cvt_pk_bf16_f32 v96, v82, v83
	v_cvt_pk_bf16_f32 v97, v84, v85
	ds_bpermute_b32 v90, v156, v94
	ds_bpermute_b32 v91, v156, v95
	ds_bpermute_b32 v92, v156, v96
	ds_bpermute_b32 v93, v156, v97
	v_add_co_u32_e32 v140, vcc, 0x38000, v170
	v_addc_co_u32_e32 v141, vcc, 0, v171, vcc
	v_mul_f32_e32 v248, 0xbfb8aa3b, v244
	v_mul_f32_e32 v250, v244, v244
	v_rcp_f32_e32 v250, v250
	v_pk_mul_f32 v[70:71], v[70:71], v[78:79]
	v_pk_mul_f32 v[72:73], v[72:73], v[80:81]
	v_pk_mul_f32 v[66:67], v[66:67], v[74:75]
	v_pk_mul_f32 v[68:69], v[68:69], v[76:77]
	v_pk_mul_f32 v[78:79], v[78:79], v[248:249] op_sel_hi:[1,0]
	v_pk_mul_f32 v[80:81], v[80:81], v[248:249] op_sel_hi:[1,0]
	v_pk_mul_f32 v[74:75], v[74:75], v[248:249] op_sel_hi:[1,0]
	v_pk_mul_f32 v[76:77], v[76:77], v[248:249] op_sel_hi:[1,0]
	v_exp_f32_e32 v78, v78
	v_exp_f32_e32 v79, v79
	v_exp_f32_e32 v80, v80
	v_exp_f32_e32 v81, v81
	v_exp_f32_e32 v74, v74
	v_exp_f32_e32 v75, v75
	v_exp_f32_e32 v76, v76
	v_exp_f32_e32 v77, v77
	v_pk_fma_f32 v[78:79], v[78:79], v[250:251], v[250:251] op_sel_hi:[1,0,0]
	v_pk_fma_f32 v[80:81], v[80:81], v[250:251], v[250:251] op_sel_hi:[1,0,0]
	v_pk_fma_f32 v[74:75], v[74:75], v[250:251], v[250:251] op_sel_hi:[1,0,0]
	v_pk_fma_f32 v[76:77], v[76:77], v[250:251], v[250:251] op_sel_hi:[1,0,0]
	v_rcp_f32_e32 v78, v78
	v_rcp_f32_e32 v79, v79
	v_rcp_f32_e32 v80, v80
	v_rcp_f32_e32 v81, v81
	v_rcp_f32_e32 v74, v74
	v_rcp_f32_e32 v75, v75
	v_rcp_f32_e32 v76, v76
	v_rcp_f32_e32 v77, v77
	v_pk_mul_f32 v[70:71], v[70:71], v[78:79]
	v_pk_mul_f32 v[72:73], v[72:73], v[80:81]
	v_pk_mul_f32 v[66:67], v[66:67], v[74:75]
	v_pk_mul_f32 v[68:69], v[68:69], v[76:77]
	s_waitcnt lgkmcnt(0)
	global_store_dwordx4 v[140:141], v[90:93], off nt
	v_cvt_pk_bf16_f32 v78, v70, v71
	v_cvt_pk_bf16_f32 v79, v72, v73
	v_cvt_pk_bf16_f32 v80, v66, v67
	v_cvt_pk_bf16_f32 v81, v68, v69
	ds_bpermute_b32 v74, v156, v78
	ds_bpermute_b32 v75, v156, v79
	ds_bpermute_b32 v76, v156, v80
	ds_bpermute_b32 v77, v156, v81
	v_add_co_u32_e32 v142, vcc, 0x54000, v170
	v_addc_co_u32_e32 v143, vcc, 0, v171, vcc
	v_mul_f32_e32 v248, 0xbfb8aa3b, v243
	v_mul_f32_e32 v250, v243, v243
	v_rcp_f32_e32 v250, v250
	v_pk_mul_f32 v[50:51], v[50:51], v[62:63]
	v_pk_mul_f32 v[52:53], v[52:53], v[64:65]
	v_pk_mul_f32 v[42:43], v[42:43], v[58:59]
	v_pk_mul_f32 v[44:45], v[44:45], v[60:61]
	v_pk_mul_f32 v[62:63], v[62:63], v[248:249] op_sel_hi:[1,0]
	v_pk_mul_f32 v[64:65], v[64:65], v[248:249] op_sel_hi:[1,0]
	v_pk_mul_f32 v[58:59], v[58:59], v[248:249] op_sel_hi:[1,0]
	v_pk_mul_f32 v[60:61], v[60:61], v[248:249] op_sel_hi:[1,0]
	v_exp_f32_e32 v62, v62
	v_exp_f32_e32 v63, v63
	v_exp_f32_e32 v64, v64
	v_exp_f32_e32 v65, v65
	v_exp_f32_e32 v58, v58
	v_exp_f32_e32 v59, v59
	v_exp_f32_e32 v60, v60
	v_exp_f32_e32 v61, v61
	v_pk_fma_f32 v[62:63], v[62:63], v[250:251], v[250:251] op_sel_hi:[1,0,0]
	v_pk_fma_f32 v[64:65], v[64:65], v[250:251], v[250:251] op_sel_hi:[1,0,0]
	v_pk_fma_f32 v[58:59], v[58:59], v[250:251], v[250:251] op_sel_hi:[1,0,0]
	v_pk_fma_f32 v[60:61], v[60:61], v[250:251], v[250:251] op_sel_hi:[1,0,0]
	v_rcp_f32_e32 v62, v62
	v_rcp_f32_e32 v63, v63
	v_rcp_f32_e32 v64, v64
	v_rcp_f32_e32 v65, v65
	v_rcp_f32_e32 v58, v58
	v_rcp_f32_e32 v59, v59
	v_rcp_f32_e32 v60, v60
	v_rcp_f32_e32 v61, v61
	v_pk_mul_f32 v[50:51], v[50:51], v[62:63]
	v_pk_mul_f32 v[52:53], v[52:53], v[64:65]
	v_pk_mul_f32 v[42:43], v[42:43], v[58:59]
	v_pk_mul_f32 v[44:45], v[44:45], v[60:61]
	s_waitcnt lgkmcnt(0)
	global_store_dwordx4 v[142:143], v[74:77], off nt
	v_cvt_pk_bf16_f32 v62, v50, v51
	v_cvt_pk_bf16_f32 v63, v52, v53
	v_cvt_pk_bf16_f32 v64, v42, v43
	v_cvt_pk_bf16_f32 v65, v44, v45
	ds_bpermute_b32 v58, v156, v62
	ds_bpermute_b32 v59, v156, v63
	ds_bpermute_b32 v60, v156, v64
	ds_bpermute_b32 v61, v156, v65
	v_add_co_u32_e32 v140, vcc, 0xe0000, v170
	v_addc_co_u32_e32 v141, vcc, 0, v171, vcc
	v_mul_f32_e32 v248, 0xbfb8aa3b, v242
	v_mul_f32_e32 v250, v242, v242
	v_rcp_f32_e32 v250, v250
	v_pk_mul_f32 v[54:55], v[54:55], v[38:39]
	v_pk_mul_f32 v[56:57], v[56:57], v[40:41]
	v_pk_mul_f32 v[46:47], v[46:47], v[34:35]
	v_pk_mul_f32 v[48:49], v[48:49], v[36:37]
	v_pk_mul_f32 v[38:39], v[38:39], v[248:249] op_sel_hi:[1,0]
	v_pk_mul_f32 v[40:41], v[40:41], v[248:249] op_sel_hi:[1,0]
	v_pk_mul_f32 v[34:35], v[34:35], v[248:249] op_sel_hi:[1,0]
	v_pk_mul_f32 v[36:37], v[36:37], v[248:249] op_sel_hi:[1,0]
	v_exp_f32_e32 v38, v38
	v_exp_f32_e32 v39, v39
	v_exp_f32_e32 v40, v40
	v_exp_f32_e32 v41, v41
	v_exp_f32_e32 v34, v34
	v_exp_f32_e32 v35, v35
	v_exp_f32_e32 v36, v36
	v_exp_f32_e32 v37, v37
	v_pk_fma_f32 v[38:39], v[38:39], v[250:251], v[250:251] op_sel_hi:[1,0,0]
	v_pk_fma_f32 v[40:41], v[40:41], v[250:251], v[250:251] op_sel_hi:[1,0,0]
	v_pk_fma_f32 v[34:35], v[34:35], v[250:251], v[250:251] op_sel_hi:[1,0,0]
	v_pk_fma_f32 v[36:37], v[36:37], v[250:251], v[250:251] op_sel_hi:[1,0,0]
	v_rcp_f32_e32 v38, v38
	v_rcp_f32_e32 v39, v39
	v_rcp_f32_e32 v40, v40
	v_rcp_f32_e32 v41, v41
	v_rcp_f32_e32 v34, v34
	v_rcp_f32_e32 v35, v35
	v_rcp_f32_e32 v36, v36
	v_rcp_f32_e32 v37, v37
	v_pk_mul_f32 v[54:55], v[54:55], v[38:39]
	v_pk_mul_f32 v[56:57], v[56:57], v[40:41]
	v_pk_mul_f32 v[46:47], v[46:47], v[34:35]
	v_pk_mul_f32 v[48:49], v[48:49], v[36:37]
	s_waitcnt lgkmcnt(0)
; __device__ __forceinline__ unsigned cvt_pk_bf16(float lo, float hi) { const f32x2c_t v = {lo, hi}; return __builtin_bit_cast(unsigned, __builtin_convertvector(v, bf16x2c_t)); }
; __device__ __forceinline__ float silu_f(float a) { return a * __builtin_amdgcn_rcpf(1.0f + __builtin_amdgcn_exp2f(a * -1.4426950408889634f)); }
;     __device__ __forceinline__ void operator()(const f32x4 (&acc)[2][2][4][2], const Unit& u, int wr, int wc, int fr, int fq) const {
;     ...
;         for (int ai = 0; ai < 2; ++ai) {
; #pragma unroll
;             for (int m = 0; m < 4; ++m) { const int row = row0 + ai * HALF + m * 16; const float rs = rs8[ai][m];
;                 const f32x4 a0 = acc[ai][0][m][0] * rs, a1 = acc[ai][0][m][1] * rs, b0 = acc[ai][1][m][0] * rs, b1 = acc[ai][1][m][1] * rs;
;                 f32x4 g0, g1;
; #pragma unroll
;                 for (int j = 0; j < 4; ++j) { g0[j] = silu_f(a0[j]) * b0[j]; g1[j] = silu_f(a1[j]) * b1[j]; }
;                 u32x4 w; w.x = cvt_pk_bf16(g0[0], g0[1]); w.y = cvt_pk_bf16(g0[2], g0[3]); w.z = cvt_pk_bf16(g1[0], g1[1]); w.w = cvt_pk_bf16(g1[2], g1[3]);
;                 w = lane_perm(w, qs4); u32x4* dst = (u32x4*)(O + (size_t)(rowS + ai * HALF + m * 16) * ldo + colS); (void)row;
;                 if constexpr (MOE) __builtin_nontemporal_store(w, dst); else *dst = w; } }
	global_store_dwordx4 v[140:141], v[58:61], off nt
	v_cvt_pk_bf16_f32 v38, v54, v55
	v_cvt_pk_bf16_f32 v39, v56, v57
	v_cvt_pk_bf16_f32 v40, v46, v47
	v_cvt_pk_bf16_f32 v41, v48, v49
	ds_bpermute_b32 v34, v156, v38
	ds_bpermute_b32 v35, v156, v39
	ds_bpermute_b32 v36, v156, v40
	ds_bpermute_b32 v37, v156, v41
	v_add_co_u32_e32 v142, vcc, 0xfc000, v170
	v_addc_co_u32_e32 v143, vcc, 0, v171, vcc
	v_mul_f32_e32 v248, 0xbfb8aa3b, v241
	v_mul_f32_e32 v250, v241, v241
	v_rcp_f32_e32 v250, v250
	v_pk_mul_f32 v[30:31], v[30:31], v[22:23]
	v_pk_mul_f32 v[32:33], v[32:33], v[24:25]
	v_pk_mul_f32 v[26:27], v[26:27], v[18:19]
	v_pk_mul_f32 v[28:29], v[28:29], v[20:21]
	v_pk_mul_f32 v[22:23], v[22:23], v[248:249] op_sel_hi:[1,0]
	v_pk_mul_f32 v[24:25], v[24:25], v[248:249] op_sel_hi:[1,0]
	v_pk_mul_f32 v[18:19], v[18:19], v[248:249] op_sel_hi:[1,0]
	v_pk_mul_f32 v[20:21], v[20:21], v[248:249] op_sel_hi:[1,0]
	v_exp_f32_e32 v22, v22
	v_exp_f32_e32 v23, v23
	v_exp_f32_e32 v24, v24
	v_exp_f32_e32 v25, v25
	v_exp_f32_e32 v18, v18
	v_exp_f32_e32 v19, v19
	v_exp_f32_e32 v20, v20
	v_exp_f32_e32 v21, v21
	v_pk_fma_f32 v[22:23], v[22:23], v[250:251], v[250:251] op_sel_hi:[1,0,0]
	v_pk_fma_f32 v[24:25], v[24:25], v[250:251], v[250:251] op_sel_hi:[1,0,0]
	v_pk_fma_f32 v[18:19], v[18:19], v[250:251], v[250:251] op_sel_hi:[1,0,0]
	v_pk_fma_f32 v[20:21], v[20:21], v[250:251], v[250:251] op_sel_hi:[1,0,0]
	v_rcp_f32_e32 v22, v22
	v_rcp_f32_e32 v23, v23
	v_rcp_f32_e32 v24, v24
	v_rcp_f32_e32 v25, v25
	v_rcp_f32_e32 v18, v18
	v_rcp_f32_e32 v19, v19
	v_rcp_f32_e32 v20, v20
	v_rcp_f32_e32 v21, v21
	v_pk_mul_f32 v[30:31], v[30:31], v[22:23]
	v_pk_mul_f32 v[32:33], v[32:33], v[24:25]
	v_pk_mul_f32 v[26:27], v[26:27], v[18:19]
	v_pk_mul_f32 v[28:29], v[28:29], v[20:21]
	s_waitcnt lgkmcnt(0)
	global_store_dwordx4 v[142:143], v[34:37], off nt
	v_cvt_pk_bf16_f32 v22, v30, v31
	v_cvt_pk_bf16_f32 v23, v32, v33
	v_cvt_pk_bf16_f32 v24, v26, v27
	v_cvt_pk_bf16_f32 v25, v28, v29
	ds_bpermute_b32 v18, v156, v22
	ds_bpermute_b32 v19, v156, v23
	ds_bpermute_b32 v20, v156, v24
	ds_bpermute_b32 v21, v156, v25
	v_add_co_u32_e32 v140, vcc, 0x118000, v170
	v_addc_co_u32_e32 v141, vcc, 0, v171, vcc
	v_mul_f32_e32 v248, 0xbfb8aa3b, v240
	v_mul_f32_e32 v250, v240, v240
	v_rcp_f32_e32 v250, v250
	v_pk_mul_f32 v[14:15], v[14:15], v[6:7]
	v_pk_mul_f32 v[16:17], v[16:17], v[8:9]
	v_pk_mul_f32 v[10:11], v[10:11], v[2:3]
	v_pk_mul_f32 v[12:13], v[12:13], v[4:5]
	v_pk_mul_f32 v[6:7], v[6:7], v[248:249] op_sel_hi:[1,0]
	v_pk_mul_f32 v[8:9], v[8:9], v[248:249] op_sel_hi:[1,0]
	v_pk_mul_f32 v[2:3], v[2:3], v[248:249] op_sel_hi:[1,0]
	v_pk_mul_f32 v[4:5], v[4:5], v[248:249] op_sel_hi:[1,0]
	v_exp_f32_e32 v6, v6
	v_exp_f32_e32 v7, v7
	v_exp_f32_e32 v8, v8
	v_exp_f32_e32 v9, v9
	v_exp_f32_e32 v2, v2
	v_exp_f32_e32 v3, v3
	v_exp_f32_e32 v4, v4
	v_exp_f32_e32 v5, v5
	v_pk_fma_f32 v[6:7], v[6:7], v[250:251], v[250:251] op_sel_hi:[1,0,0]
	v_pk_fma_f32 v[8:9], v[8:9], v[250:251], v[250:251] op_sel_hi:[1,0,0]
	v_pk_fma_f32 v[2:3], v[2:3], v[250:251], v[250:251] op_sel_hi:[1,0,0]
	v_pk_fma_f32 v[4:5], v[4:5], v[250:251], v[250:251] op_sel_hi:[1,0,0]
	v_rcp_f32_e32 v6, v6
	v_rcp_f32_e32 v7, v7
	v_rcp_f32_e32 v8, v8
	v_rcp_f32_e32 v9, v9
	v_rcp_f32_e32 v2, v2
	v_rcp_f32_e32 v3, v3
	v_rcp_f32_e32 v4, v4
	v_rcp_f32_e32 v5, v5
	v_pk_mul_f32 v[14:15], v[14:15], v[6:7]
	v_pk_mul_f32 v[16:17], v[16:17], v[8:9]
	v_pk_mul_f32 v[10:11], v[10:11], v[2:3]
	v_pk_mul_f32 v[12:13], v[12:13], v[4:5]
	s_waitcnt lgkmcnt(0)
	global_store_dwordx4 v[140:141], v[18:21], off nt
	v_cvt_pk_bf16_f32 v6, v14, v15
	v_cvt_pk_bf16_f32 v7, v16, v17
	v_cvt_pk_bf16_f32 v8, v10, v11
	v_cvt_pk_bf16_f32 v9, v12, v13
	ds_bpermute_b32 v2, v156, v6
	ds_bpermute_b32 v3, v156, v7
	ds_bpermute_b32 v4, v156, v8
	ds_bpermute_b32 v5, v156, v9
	v_add_co_u32_e32 v142, vcc, 0x134000, v170
	v_addc_co_u32_e32 v143, vcc, 0, v171, vcc
	s_waitcnt lgkmcnt(0)
	global_store_dwordx4 v[142:143], v[2:5], off nt
	s_and_b64 vcc, exec, s[4:5]
	s_mov_b64 s[4:5], -1
	s_cbranch_vccnz .LBB0_1718
	s_andn2_b64 vcc, exec, s[10:11]
	s_cbranch_vccnz .LBB0_1717
	s_barrier
	s_branch .LBB0_1717
